# v048 + fold stats chain rewritten: 8/2 dwordx4 loads instead of 32 branch-guarded dword loads, exact 2^-k multiply instead of IEEE divide by power-of-two n (bit-identical), part pointer s_load hoisted
# baseline (speedup 1.0000x reference)
_Z11fold_kernelPKfS0_S0_S0_S0_S0_S0_S0_S0_PDv4_jPf:
	s_load_dwordx2 s[24:25], s[0:1], 0x0
	s_load_dwordx8 s[8:15], s[0:1], 0x8
	s_load_dwordx2 s[18:19], s[0:1], 0x28
	s_load_dwordx2 s[20:21], s[0:1], 0x38
	s_lshl_b32 s16, s2, 5
	s_lshl_b32 s5, s3, 7
	v_and_b32_e32 v53, 31, v0
	s_cmp_eq_u32 s4, 0
	v_lshrrev_b32_e32 v52, 6, v0
	s_cselect_b64 s[6:7], -1, 0
	v_or_b32_e32 v18, s16, v53
	v_lshrrev_b32_e32 v1, 2, v0
	s_and_b64 s[22:23], s[6:7], exec
	v_and_b32_e32 v54, 8, v1
	v_ashrrev_i32_e32 v19, 31, v18
	v_lshlrev_b32_e32 v55, 4, v52
	s_waitcnt lgkmcnt(0)
	s_cselect_b32 s19, s19, s21
	s_cselect_b32 s18, s18, s20
	v_lshlrev_b64 v[2:3], 11, v[18:19]
	v_or3_b32 v4, s5, v55, v54
	v_lshl_add_u64 v[2:3], s[18:19], 0, v[2:3]
	v_ashrrev_i32_e32 v5, 31, v4
	v_lshl_add_u64 v[10:11], v[4:5], 2, v[2:3]
	v_or_b32_e32 v4, 64, v4
	v_ashrrev_i32_e32 v5, 31, v4
	v_lshl_add_u64 v[20:21], v[4:5], 2, v[2:3]
	v_and_b32_e32 v58, 0x7f, v0
	global_load_dwordx4 v[6:9], v[10:11], off offset:16
	global_load_dwordx4 v[14:17], v[10:11], off
	global_load_dwordx4 v[2:5], v[20:21], off offset:16
	s_nop 0
	global_load_dwordx4 v[10:13], v[20:21], off
	v_or_b32_e32 v20, s5, v58
	v_ashrrev_i32_e32 v21, 31, v20
	s_cselect_b32 s9, s9, s13
	s_cselect_b32 s8, s8, s12
	s_cselect_b32 s11, s11, s15
	s_cselect_b32 s10, s10, s14
	v_lshlrev_b64 v[20:21], 2, v[20:21]
	v_lshl_add_u64 v[22:23], s[8:9], 0, v[20:21]
	v_lshl_add_u64 v[20:21], s[10:11], 0, v[20:21]
	global_load_dword v57, v[22:23], off
	global_load_dword v56, v[20:21], off
	s_cmp_lg_u32 s3, 0
	v_mov_b32_e32 v1, 0
	s_cbranch_scc0 .LBB1_76
	v_cmp_lt_u32_e32 vcc, 31, v0
	s_and_saveexec_b64 s[8:9], vcc
	s_xor_b64 s[8:9], exec, s[8:9]

.LBB1_3:
	s_or_saveexec_b64 s[10:11], s[8:9]
	s_load_dwordx2 s[8:9], s[0:1], 0x50
	v_mov_b32_e32 v18, s5
	s_xor_b64 exec, exec, s[10:11]
	s_cbranch_execz .LBB1_65
	s_lshl_b32 s5, s3, 3
	v_and_b32_e32 v60, 7, v0
	v_lshrrev_b32_e32 v59, 3, v0
	v_or_b32_e32 v20, s5, v60
	s_and_b64 s[14:15], s[6:7], exec
	s_cselect_b32 s14, 0, 16
	v_lshlrev_b32_e32 v18, 5, v59
	v_mov_b32_e32 v19, 0
	v_ashrrev_i32_e32 v21, 31, v20
	v_lshl_add_u64 v[20:21], v[18:19], 0, v[20:21]
	v_mov_b32_e32 v18, s14
	v_mad_u64_u32 v[22:23], s[18:19], v20, 20, v[18:19]
	v_mad_i32_i24 v23, v21, 20, v23
	s_waitcnt lgkmcnt(0)
	v_lshl_add_u64 v[22:23], v[22:23], 3, s[24:25]
	s_cmp_eq_u32 s4, 0
	s_cbranch_scc1 .Lfold_video
	global_load_dwordx4 v[24:27], v[22:23], off
	global_load_dwordx4 v[28:31], v[22:23], off offset:16
	v_mov_b32_e32 v32, 0
	v_mov_b32_e32 v33, 0
	v_mov_b32_e32 v34, 0
	v_mov_b32_e32 v35, 0
	v_mov_b32_e32 v36, 0
	v_mov_b32_e32 v37, 0
	v_mov_b32_e32 v38, 0
	v_mov_b32_e32 v39, 0
	v_mov_b32_e32 v40, 0
	v_mov_b32_e32 v41, 0
	v_mov_b32_e32 v42, 0
	v_mov_b32_e32 v43, 0
	v_mov_b32_e32 v44, 0
	v_mov_b32_e32 v45, 0
	v_mov_b32_e32 v46, 0
	v_mov_b32_e32 v47, 0
	v_mov_b32_e32 v48, 0
	v_mov_b32_e32 v49, 0
	v_mov_b32_e32 v50, 0
	v_mov_b32_e32 v51, 0
	v_mov_b32_e32 v18, 0
	v_mov_b32_e32 v19, 0
	v_mov_b32_e32 v20, 0
	v_mov_b32_e32 v21, 0
	s_branch .Lfold_join
.Lfold_video:
	global_load_dwordx4 v[24:27], v[22:23], off
	global_load_dwordx4 v[28:31], v[22:23], off offset:16
	global_load_dwordx4 v[32:35], v[22:23], off offset:32
	global_load_dwordx4 v[36:39], v[22:23], off offset:48
	global_load_dwordx4 v[40:43], v[22:23], off offset:64
	global_load_dwordx4 v[44:47], v[22:23], off offset:80
	global_load_dwordx4 v[48:51], v[22:23], off offset:96
	global_load_dwordx4 v[18:21], v[22:23], off offset:112
.Lfold_join:
	s_waitcnt vmcnt(0)
	v_pk_add_f32 v[24:25], v[24:25], 0 op_sel_hi:[1,0]
	s_nop 0
	v_pk_add_f32 v[24:25], v[24:25], v[26:27]
	s_nop 0
	v_pk_add_f32 v[24:25], v[24:25], v[28:29]
	s_nop 0
	v_pk_add_f32 v[24:25], v[24:25], v[30:31]
	s_nop 0
	v_pk_add_f32 v[24:25], v[24:25], v[32:33]
	s_nop 0
	v_pk_add_f32 v[24:25], v[24:25], v[34:35]
	s_nop 0
	v_pk_add_f32 v[24:25], v[24:25], v[36:37]
	s_nop 0
	v_pk_add_f32 v[24:25], v[24:25], v[38:39]
	s_nop 0
	v_pk_add_f32 v[24:25], v[24:25], v[40:41]
	s_nop 0
	v_pk_add_f32 v[24:25], v[24:25], v[42:43]
	s_nop 0
	v_pk_add_f32 v[24:25], v[24:25], v[44:45]
	s_nop 0
	v_pk_add_f32 v[24:25], v[24:25], v[46:47]
	s_nop 0
	v_pk_add_f32 v[24:25], v[24:25], v[48:49]
	s_nop 0
	v_pk_add_f32 v[24:25], v[24:25], v[50:51]
	s_nop 0
	v_pk_add_f32 v[24:25], v[24:25], v[18:19]
	s_nop 0
	v_pk_add_f32 v[24:25], v[24:25], v[20:21]
	s_nop 0
	v_mov_b32_e32 v20, 0x38800000
	v_mov_b32_e32 v21, 0x37800000
	v_cndmask_b32_e64 v20, v20, v21, s[6:7]
	v_mul_f32_e32 v19, v24, v20
	v_mul_f32_e32 v18, v25, v20
	s_mov_b32 s6, 0x800000
	v_fma_f32 v18, -v19, v19, v18
	v_max_f32_e32 v18, 0, v18
	v_add_f32_e32 v18, 0x3727c5ac, v18
	v_mul_f32_e32 v20, 0x4b800000, v18
	v_cmp_gt_f32_e32 vcc, s6, v18
	s_nop 1
	v_cndmask_b32_e32 v18, v18, v20, vcc
	v_rsq_f32_e32 v18, v18
	v_lshlrev_b32_e32 v20, 2, v60
	v_lshl_or_b32 v20, v59, 5, v20
	v_add_u32_e32 v20, 0x1800, v20
	v_mul_f32_e32 v21, 0x45800000, v18
	v_cndmask_b32_e32 v18, v18, v21, vcc
	ds_write2_b32 v20, v19, v18 offset1:32
	v_mov_b32_e32 v18, s5

	.amdhsa_kernel _Z11fold_kernelPKfS0_S0_S0_S0_S0_S0_S0_S0_PDv4_jPf
		.amdhsa_group_segment_fixed_size 6400
		.amdhsa_private_segment_fixed_size 0
		.amdhsa_kernarg_size 88
		.amdhsa_user_sgpr_count 2
		.amdhsa_user_sgpr_dispatch_ptr 0
		.amdhsa_user_sgpr_queue_ptr 0
		.amdhsa_user_sgpr_kernarg_segment_ptr 1
		.amdhsa_user_sgpr_dispatch_id 0
		.amdhsa_user_sgpr_kernarg_preload_length 0
		.amdhsa_user_sgpr_kernarg_preload_offset 0
		.amdhsa_user_sgpr_private_segment_size 0
		.amdhsa_uses_dynamic_stack 0
		.amdhsa_enable_private_segment 0
		.amdhsa_system_sgpr_workgroup_id_x 1
		.amdhsa_system_sgpr_workgroup_id_y 1
		.amdhsa_system_sgpr_workgroup_id_z 1
		.amdhsa_system_sgpr_workgroup_info 0
		.amdhsa_system_vgpr_workitem_id 0
		.amdhsa_next_free_vgpr 72
		.amdhsa_next_free_sgpr 26
		.amdhsa_accum_offset 72
		.amdhsa_reserve_vcc 1
		.amdhsa_float_round_mode_32 0
		.amdhsa_float_round_mode_16_64 0
		.amdhsa_float_denorm_mode_32 3
		.amdhsa_float_denorm_mode_16_64 3
		.amdhsa_dx10_clamp 1
		.amdhsa_ieee_mode 1
		.amdhsa_fp16_overflow 0
		.amdhsa_tg_split 0
		.amdhsa_exception_fp_ieee_invalid_op 0
		.amdhsa_exception_fp_denorm_src 0
		.amdhsa_exception_fp_ieee_div_zero 0
		.amdhsa_exception_fp_ieee_overflow 0
		.amdhsa_exception_fp_ieee_underflow 0
		.amdhsa_exception_fp_ieee_inexact 0
		.amdhsa_exception_int_div_zero 0
	.end_amdhsa_kernel

amdhsa.kernels:
  - .agpr_count:     0
    .args:
      - .actual_access:  read_only
        .address_space:  global
        .offset:         0
        .size:           8
        .value_kind:     global_buffer
      - .actual_access:  read_only
        .address_space:  global
        .offset:         8
        .size:           8
        .value_kind:     global_buffer
      - .actual_access:  write_only
        .address_space:  global
        .offset:         16
        .size:           8
        .value_kind:     global_buffer
      - .actual_access:  write_only
        .address_space:  global
        .offset:         24
        .size:           8
        .value_kind:     global_buffer
      - .actual_access:  write_only
        .address_space:  global
        .offset:         32
        .size:           8
        .value_kind:     global_buffer
    .group_segment_fixed_size: 32896
    .kernarg_segment_align: 8
    .kernarg_segment_size: 40
    .language:       OpenCL C
    .language_version:
      - 2
      - 0
    .max_flat_workgroup_size: 256
    .name:           _Z11prep_kernelPKfS0_PDv4_jS2_Pf
    .private_segment_fixed_size: 0
    .sgpr_count:     19
    .sgpr_spill_count: 0
    .symbol:         _Z11prep_kernelPKfS0_PDv4_jS2_Pf.kd
    .uniform_work_group_size: 1
    .uses_dynamic_stack: false
    .vgpr_count:     115
    .vgpr_spill_count: 0
    .wavefront_size: 64
  - .agpr_count:     0
    .args:
      - .actual_access:  read_only
        .address_space:  global
        .offset:         0
        .size:           8
        .value_kind:     global_buffer
      - .actual_access:  read_only
        .address_space:  global
        .offset:         8
        .size:           8
        .value_kind:     global_buffer
      - .actual_access:  read_only
        .address_space:  global
        .offset:         16
        .size:           8
        .value_kind:     global_buffer
      - .actual_access:  read_only
        .address_space:  global
        .offset:         24
        .size:           8
        .value_kind:     global_buffer
      - .actual_access:  read_only
        .address_space:  global
        .offset:         32
        .size:           8
        .value_kind:     global_buffer
      - .actual_access:  read_only
        .address_space:  global
        .offset:         40
        .size:           8
        .value_kind:     global_buffer
      - .actual_access:  read_only
        .address_space:  global
        .offset:         48
        .size:           8
        .value_kind:     global_buffer
      - .actual_access:  read_only
        .address_space:  global
        .offset:         56
        .size:           8
        .value_kind:     global_buffer
      - .actual_access:  read_only
        .address_space:  global
        .offset:         64
        .size:           8
        .value_kind:     global_buffer
      - .actual_access:  write_only
        .address_space:  global
        .offset:         72
        .size:           8
        .value_kind:     global_buffer
      - .actual_access:  write_only
        .address_space:  global
        .offset:         80
        .size:           8
        .value_kind:     global_buffer
    .group_segment_fixed_size: 6400
    .kernarg_segment_align: 8
    .kernarg_segment_size: 88
    .language:       OpenCL C
    .language_version:
      - 2
      - 0
    .max_flat_workgroup_size: 256
    .name:           _Z11fold_kernelPKfS0_S0_S0_S0_S0_S0_S0_S0_PDv4_jPf
    .private_segment_fixed_size: 0
    .sgpr_count:     32
    .sgpr_spill_count: 0
    .symbol:         _Z11fold_kernelPKfS0_S0_S0_S0_S0_S0_S0_S0_PDv4_jPf.kd
    .uniform_work_group_size: 1
    .uses_dynamic_stack: false
    .vgpr_count:     72
    .vgpr_spill_count: 0
    .wavefront_size: 64
  - .agpr_count:     0
    .args:
      - .actual_access:  read_only
        .address_space:  global
        .offset:         0
        .size:           8
        .value_kind:     global_buffer
      - .actual_access:  read_only
        .address_space:  global
        .offset:         8
        .size:           8
        .value_kind:     global_buffer
      - .actual_access:  read_only
        .address_space:  global
        .offset:         16
        .size:           8
        .value_kind:     global_buffer
      - .actual_access:  write_only
        .address_space:  global
        .offset:         24
        .size:           8
        .value_kind:     global_buffer
    .group_segment_fixed_size: 37888
    .kernarg_segment_align: 8
    .kernarg_segment_size: 32
    .language:       OpenCL C
    .language_version:
      - 2
      - 0
    .max_flat_workgroup_size: 512
    .name:           _Z17audio_proj_kernelPKDv4_jS1_PKfPS_
    .private_segment_fixed_size: 0
    .sgpr_count:     22
    .sgpr_spill_count: 0
    .symbol:         _Z17audio_proj_kernelPKDv4_jS1_PKfPS_.kd
    .uniform_work_group_size: 1
    .uses_dynamic_stack: false
    .vgpr_count:     150
    .vgpr_spill_count: 0
    .wavefront_size: 64
  - .agpr_count:     0
    .args:
      - .actual_access:  read_only
        .address_space:  global
        .offset:         0
        .size:           8
        .value_kind:     global_buffer
      - .actual_access:  read_only
        .address_space:  global
        .offset:         8
        .size:           8
        .value_kind:     global_buffer
      - .actual_access:  read_only
        .address_space:  global
        .offset:         16
        .size:           8
        .value_kind:     global_buffer
      - .actual_access:  read_only
        .address_space:  global
        .offset:         24
        .size:           8
        .value_kind:     global_buffer
      - .actual_access:  read_only
        .address_space:  global
        .offset:         32
        .size:           8
        .value_kind:     global_buffer
      - .actual_access:  read_only
        .address_space:  global
        .offset:         40
        .size:           8
        .value_kind:     global_buffer
      - .actual_access:  write_only
        .address_space:  global
        .offset:         48
        .size:           8
        .value_kind:     global_buffer
      - .actual_access:  write_only
        .address_space:  global
        .offset:         56
        .size:           8
        .value_kind:     global_buffer
    .group_segment_fixed_size: 124928
    .kernarg_segment_align: 8
    .kernarg_segment_size: 64
    .language:       OpenCL C
    .language_version:
      - 2
      - 0
    .max_flat_workgroup_size: 512
    .name:           _Z12fused_kernelPKDv4_jS1_S1_PKfS3_S3_PfS4_
    .private_segment_fixed_size: 0
    .sgpr_count:     50
    .sgpr_spill_count: 0
    .symbol:         _Z12fused_kernelPKDv4_jS1_S1_PKfS3_S3_PfS4_.kd
    .uniform_work_group_size: 1
    .uses_dynamic_stack: false
    .vgpr_count:     256
    .vgpr_spill_count: 0
    .wavefront_size: 64
